# layer-0 PEER row pass (residual add + next-layer norm): all 24 row loads (x, gate, F) issued up front and the 16 modulation loads issued together before the row reduction, instead of one load-wait-sto
# speedup vs baseline: 1.0099x; 1.0074x over previous
.LBB0_1679:
	v_cmp_gt_i32_e32 vcc, s18, v64
	v_ashrrev_i32_e32 v65, 31, v64
	s_mov_b64 s[12:13], 0x10a000
	v_cndmask_b32_e64 v192, v216, 0, vcc
	v_lshl_add_u64 v[30:31], s[0:1], 0, v[192:193]
	v_lshlrev_b64 v[86:87], 12, v[64:65]
	v_lshl_add_u64 v[58:59], v[30:31], 0, s[12:13]
	v_lshlrev_b64 v[30:31], 13, v[64:65]
	v_lshl_add_u64 v[92:93], v[78:79], 0, v[86:87]
	v_lshl_add_u64 v[60:61], s[6:7], 0, v[30:31]
	v_mov_b32_e32 v63, v193
	v_lshl_add_u64 v[46:47], v[60:61], 0, v[62:63]
	v_lshl_add_u64 v[34:35], v[58:59], 0, v[62:63]
	v_mov_b32_e32 v67, v193
	v_mov_b32_e32 v69, v193
	v_mov_b32_e32 v71, v193
	v_mov_b32_e32 v73, v193
	v_mov_b32_e32 v75, v193
	v_lshl_add_u64 v[110:111], v[60:61], 0, v[74:75]
	v_mov_b32_e32 v77, v193
	v_lshl_add_u64 v[118:119], v[60:61], 0, v[76:77]
	v_mov_b32_e32 v85, v193
	v_lshl_add_u64 v[86:87], v[80:81], 0, v[86:87]
	v_mov_b32_e32 v65, 0
	global_load_dwordx2 v[160:161], v[92:93], off
	global_load_dwordx2 v[162:163], v[92:93], off offset:512
	global_load_dwordx2 v[164:165], v[92:93], off offset:1024
	global_load_dwordx2 v[166:167], v[92:93], off offset:1536
	global_load_dwordx2 v[168:169], v[92:93], off offset:2048
	global_load_dwordx2 v[170:171], v[92:93], off offset:2560
	global_load_dwordx2 v[172:173], v[92:93], off offset:3072
	global_load_dwordx2 v[174:175], v[92:93], off offset:3584
	v_lshl_add_u64 v[30:31], v[60:61], 0, v[62:63]
	global_load_dwordx4 v[128:131], v[30:31], off
	v_lshl_add_u64 v[252:253], v[58:59], 0, v[62:63]
	global_load_dwordx4 v[218:221], v[252:253], off
	v_lshl_add_u64 v[32:33], v[60:61], 0, v[66:67]
	global_load_dwordx4 v[132:135], v[32:33], off
	v_lshl_add_u64 v[252:253], v[58:59], 0, v[66:67]
	global_load_dwordx4 v[222:225], v[252:253], off
	v_lshl_add_u64 v[34:35], v[60:61], 0, v[68:69]
	global_load_dwordx4 v[136:139], v[34:35], off
	v_lshl_add_u64 v[252:253], v[58:59], 0, v[68:69]
	global_load_dwordx4 v[226:229], v[252:253], off
	v_lshl_add_u64 v[36:37], v[60:61], 0, v[70:71]
	global_load_dwordx4 v[140:143], v[36:37], off
	v_lshl_add_u64 v[252:253], v[58:59], 0, v[70:71]
	global_load_dwordx4 v[230:233], v[252:253], off
	v_lshl_add_u64 v[38:39], v[60:61], 0, v[72:73]
	global_load_dwordx4 v[144:147], v[38:39], off
	v_lshl_add_u64 v[252:253], v[58:59], 0, v[72:73]
	global_load_dwordx4 v[234:237], v[252:253], off
	v_lshl_add_u64 v[40:41], v[60:61], 0, v[74:75]
	global_load_dwordx4 v[148:151], v[40:41], off
	v_lshl_add_u64 v[252:253], v[58:59], 0, v[74:75]
	global_load_dwordx4 v[238:241], v[252:253], off
	v_lshl_add_u64 v[42:43], v[60:61], 0, v[76:77]
	global_load_dwordx4 v[152:155], v[42:43], off
	v_lshl_add_u64 v[252:253], v[58:59], 0, v[76:77]
	global_load_dwordx4 v[242:245], v[252:253], off
	v_lshl_add_u64 v[44:45], v[60:61], 0, v[84:85]
	global_load_dwordx4 v[156:159], v[44:45], off
	v_lshl_add_u64 v[252:253], v[58:59], 0, v[84:85]
	global_load_dwordx4 v[246:249], v[252:253], off
	v_lshl_add_u64 v[98:99], s[8:9], 0, v[192:193]
	v_lshl_add_u64 v[100:101], v[98:99], 0, s[40:41]
	s_waitcnt vmcnt(14)
	v_lshlrev_b32_e32 v104, 16, v160
	v_and_b32_e32 v105, 0xffff0000, v160
	v_lshlrev_b32_e32 v106, 16, v161
	v_and_b32_e32 v107, 0xffff0000, v161
	v_fmac_f32_e32 v128, v218, v104
	v_fmac_f32_e32 v129, v219, v105
	v_fmac_f32_e32 v130, v220, v106
	v_fmac_f32_e32 v131, v221, v107
	global_store_dwordx4 v[30:31], v[128:131], off
	v_fmac_f32_e32 v65, v128, v128
	v_fmac_f32_e32 v65, v129, v129
	v_fmac_f32_e32 v65, v130, v130
	v_fmac_f32_e32 v65, v131, v131
	s_waitcnt vmcnt(13)
	v_lshlrev_b32_e32 v104, 16, v162
	v_and_b32_e32 v105, 0xffff0000, v162
	v_lshlrev_b32_e32 v106, 16, v163
	v_and_b32_e32 v107, 0xffff0000, v163
	v_fmac_f32_e32 v132, v222, v104
	v_fmac_f32_e32 v133, v223, v105
	v_fmac_f32_e32 v134, v224, v106
	v_fmac_f32_e32 v135, v225, v107
	global_store_dwordx4 v[32:33], v[132:135], off
	v_fmac_f32_e32 v65, v132, v132
	v_fmac_f32_e32 v65, v133, v133
	v_fmac_f32_e32 v65, v134, v134
	v_fmac_f32_e32 v65, v135, v135
	s_waitcnt vmcnt(12)
	v_lshlrev_b32_e32 v104, 16, v164
	v_and_b32_e32 v105, 0xffff0000, v164
	v_lshlrev_b32_e32 v106, 16, v165
	v_and_b32_e32 v107, 0xffff0000, v165
	v_fmac_f32_e32 v136, v226, v104
	v_fmac_f32_e32 v137, v227, v105
	v_fmac_f32_e32 v138, v228, v106
	v_fmac_f32_e32 v139, v229, v107
	global_store_dwordx4 v[34:35], v[136:139], off
	v_fmac_f32_e32 v65, v136, v136
	v_fmac_f32_e32 v65, v137, v137
	v_fmac_f32_e32 v65, v138, v138
	v_fmac_f32_e32 v65, v139, v139
	s_waitcnt vmcnt(11)
	v_lshlrev_b32_e32 v104, 16, v166
	v_and_b32_e32 v105, 0xffff0000, v166
	v_lshlrev_b32_e32 v106, 16, v167
	v_and_b32_e32 v107, 0xffff0000, v167
	v_fmac_f32_e32 v140, v230, v104
	v_fmac_f32_e32 v141, v231, v105
	v_fmac_f32_e32 v142, v232, v106
	v_fmac_f32_e32 v143, v233, v107
	global_store_dwordx4 v[36:37], v[140:143], off
	v_fmac_f32_e32 v65, v140, v140
	v_fmac_f32_e32 v65, v141, v141
	v_fmac_f32_e32 v65, v142, v142
	v_fmac_f32_e32 v65, v143, v143
	s_waitcnt vmcnt(10)
	v_lshlrev_b32_e32 v104, 16, v168
	v_and_b32_e32 v105, 0xffff0000, v168
	v_lshlrev_b32_e32 v106, 16, v169
	v_and_b32_e32 v107, 0xffff0000, v169
	v_fmac_f32_e32 v144, v234, v104
	v_fmac_f32_e32 v145, v235, v105
	v_fmac_f32_e32 v146, v236, v106
	v_fmac_f32_e32 v147, v237, v107
	global_store_dwordx4 v[38:39], v[144:147], off
	v_fmac_f32_e32 v65, v144, v144
	v_fmac_f32_e32 v65, v145, v145
	v_fmac_f32_e32 v65, v146, v146
	v_fmac_f32_e32 v65, v147, v147
	s_waitcnt vmcnt(9)
	v_lshlrev_b32_e32 v104, 16, v170
	v_and_b32_e32 v105, 0xffff0000, v170
	v_lshlrev_b32_e32 v106, 16, v171
	v_and_b32_e32 v107, 0xffff0000, v171
	v_fmac_f32_e32 v148, v238, v104
	v_fmac_f32_e32 v149, v239, v105
	v_fmac_f32_e32 v150, v240, v106
	v_fmac_f32_e32 v151, v241, v107
	global_store_dwordx4 v[40:41], v[148:151], off
	v_fmac_f32_e32 v65, v148, v148
	v_fmac_f32_e32 v65, v149, v149
	v_fmac_f32_e32 v65, v150, v150
	v_fmac_f32_e32 v65, v151, v151
	s_waitcnt vmcnt(8)
	v_lshlrev_b32_e32 v104, 16, v172
	v_and_b32_e32 v105, 0xffff0000, v172
	v_lshlrev_b32_e32 v106, 16, v173
	v_and_b32_e32 v107, 0xffff0000, v173
	v_fmac_f32_e32 v152, v242, v104
	v_fmac_f32_e32 v153, v243, v105
	v_fmac_f32_e32 v154, v244, v106
	v_fmac_f32_e32 v155, v245, v107
	global_store_dwordx4 v[42:43], v[152:155], off
	v_fmac_f32_e32 v65, v152, v152
	v_fmac_f32_e32 v65, v153, v153
	v_fmac_f32_e32 v65, v154, v154
	v_fmac_f32_e32 v65, v155, v155
	s_waitcnt vmcnt(7)
	v_lshlrev_b32_e32 v104, 16, v174
	v_and_b32_e32 v105, 0xffff0000, v174
	v_lshlrev_b32_e32 v106, 16, v175
	v_and_b32_e32 v107, 0xffff0000, v175
	v_fmac_f32_e32 v156, v246, v104
	v_fmac_f32_e32 v157, v247, v105
	v_fmac_f32_e32 v158, v248, v106
	v_fmac_f32_e32 v159, v249, v107
	global_store_dwordx4 v[44:45], v[156:159], off
	v_fmac_f32_e32 v65, v156, v156
	v_fmac_f32_e32 v65, v157, v157
	v_fmac_f32_e32 v65, v158, v158
	v_fmac_f32_e32 v65, v159, v159
	v_lshl_add_u64 v[250:251], v[98:99], 0, v[62:63]
	global_load_dwordx4 v[218:221], v[250:251], off
	v_lshl_add_u64 v[252:253], v[100:101], 0, v[62:63]
	global_load_dwordx4 v[176:179], v[252:253], off
	v_lshl_add_u64 v[250:251], v[98:99], 0, v[66:67]
	global_load_dwordx4 v[222:225], v[250:251], off
	v_lshl_add_u64 v[252:253], v[100:101], 0, v[66:67]
	global_load_dwordx4 v[180:183], v[252:253], off
	v_lshl_add_u64 v[250:251], v[98:99], 0, v[68:69]
	global_load_dwordx4 v[226:229], v[250:251], off
	v_lshl_add_u64 v[252:253], v[100:101], 0, v[68:69]
	global_load_dwordx4 v[184:187], v[252:253], off
	v_lshl_add_u64 v[250:251], v[98:99], 0, v[70:71]
	global_load_dwordx4 v[230:233], v[250:251], off
	v_lshl_add_u64 v[252:253], v[100:101], 0, v[70:71]
	global_load_dwordx4 v[188:191], v[252:253], off
	v_lshl_add_u64 v[250:251], v[98:99], 0, v[72:73]
	global_load_dwordx4 v[234:237], v[250:251], off
	v_lshl_add_u64 v[252:253], v[100:101], 0, v[72:73]
	global_load_dwordx4 v[200:203], v[252:253], off
	v_lshl_add_u64 v[250:251], v[98:99], 0, v[74:75]
	global_load_dwordx4 v[238:241], v[250:251], off
	v_lshl_add_u64 v[252:253], v[100:101], 0, v[74:75]
	global_load_dwordx4 v[204:207], v[252:253], off
	v_lshl_add_u64 v[250:251], v[98:99], 0, v[76:77]
	global_load_dwordx4 v[242:245], v[250:251], off
	v_lshl_add_u64 v[252:253], v[100:101], 0, v[76:77]
	global_load_dwordx4 v[208:211], v[252:253], off
	v_lshl_add_u64 v[250:251], v[98:99], 0, v[84:85]
	global_load_dwordx4 v[246:249], v[250:251], off
	v_lshl_add_u64 v[252:253], v[100:101], 0, v[84:85]
	global_load_dwordx4 v[212:215], v[252:253], off
	s_nop 1
	v_add_f32_dpp v65, v65, v65 quad_perm:[1,0,3,2] row_mask:0xf bank_mask:0xf bound_ctrl:1
	s_nop 1
	v_add_f32_dpp v65, v65, v65 quad_perm:[2,3,0,1] row_mask:0xf bank_mask:0xf bound_ctrl:1
	s_nop 1
	v_add_f32_dpp v65, v65, v65 row_half_mirror row_mask:0xf bank_mask:0xf bound_ctrl:1
	s_nop 1
	v_add_f32_dpp v65, v65, v65 row_mirror row_mask:0xf bank_mask:0xf bound_ctrl:1
	ds_swizzle_b32 v88, v65 offset:swizzle(SWAP,16)
	s_waitcnt lgkmcnt(0)
	v_add_f32_e32 v65, v65, v88
	s_nop 0
	v_readlane_b32 s13, v65, 32
	v_readlane_b32 s12, v65, 0
	s_nop 0
	v_mov_b32_e32 v65, s13
	v_add_f32_e32 v65, s12, v65
	v_fmamk_f32 v65, v65, 0x3a000000, v124
	v_cmp_gt_f32_e32 vcc, s20, v65
	v_mul_f32_e32 v88, 0x4b800000, v65
	s_nop 0
	v_cndmask_b32_e32 v65, v65, v88, vcc
	v_rsq_f32_e32 v65, v65
	s_nop 0
	v_mul_f32_e32 v88, 0x45800000, v65
	v_cndmask_b32_e32 v96, v65, v88, vcc
	s_waitcnt vmcnt(14)
	v_mul_f32_e32 v104, v128, v96
	v_mul_f32_e32 v105, v129, v96
	v_mul_f32_e32 v106, v130, v96
	v_mul_f32_e32 v107, v131, v96
	v_mul_f32_e32 v104, v0, v104
	v_mul_f32_e32 v105, v82, v105
	v_mul_f32_e32 v106, v1, v106
	v_mul_f32_e32 v107, v83, v107
	v_add_f32_e32 v108, 1.0, v176
	v_add_f32_e32 v109, 1.0, v177
	v_add_f32_e32 v110, 1.0, v178
	v_add_f32_e32 v111, 1.0, v179
	v_fma_f32 v104, v108, v104, v218
	v_fma_f32 v105, v109, v105, v219
	v_fma_f32 v106, v110, v106, v220
	v_fma_f32 v107, v111, v107, v221
	v_cvt_pk_bf16_f32 v112, v104, v105
	v_cvt_pk_bf16_f32 v113, v106, v107
	global_store_dwordx2 v[86:87], v[112:113], off
	s_waitcnt vmcnt(13)
	v_mul_f32_e32 v104, v132, v96
	v_mul_f32_e32 v105, v133, v96
	v_mul_f32_e32 v106, v134, v96
	v_mul_f32_e32 v107, v135, v96
	v_mul_f32_e32 v104, v4, v104
	v_mul_f32_e32 v105, v2, v105
	v_mul_f32_e32 v106, v5, v106
	v_mul_f32_e32 v107, v3, v107
	v_add_f32_e32 v108, 1.0, v180
	v_add_f32_e32 v109, 1.0, v181
	v_add_f32_e32 v110, 1.0, v182
	v_add_f32_e32 v111, 1.0, v183
	v_fma_f32 v104, v108, v104, v222
	v_fma_f32 v105, v109, v105, v223
	v_fma_f32 v106, v110, v106, v224
	v_fma_f32 v107, v111, v107, v225
	v_cvt_pk_bf16_f32 v114, v104, v105
	v_cvt_pk_bf16_f32 v115, v106, v107
	global_store_dwordx2 v[86:87], v[114:115], off offset:512
	s_waitcnt vmcnt(12)
	v_mul_f32_e32 v104, v136, v96
	v_mul_f32_e32 v105, v137, v96
	v_mul_f32_e32 v106, v138, v96
	v_mul_f32_e32 v107, v139, v96
	v_mul_f32_e32 v104, v8, v104
	v_mul_f32_e32 v105, v6, v105
	v_mul_f32_e32 v106, v9, v106
	v_mul_f32_e32 v107, v7, v107
	v_add_f32_e32 v108, 1.0, v184
	v_add_f32_e32 v109, 1.0, v185
	v_add_f32_e32 v110, 1.0, v186
	v_add_f32_e32 v111, 1.0, v187
	v_fma_f32 v104, v108, v104, v226
	v_fma_f32 v105, v109, v105, v227
	v_fma_f32 v106, v110, v106, v228
	v_fma_f32 v107, v111, v107, v229
	v_cvt_pk_bf16_f32 v112, v104, v105
	v_cvt_pk_bf16_f32 v113, v106, v107
	global_store_dwordx2 v[86:87], v[112:113], off offset:1024
	s_waitcnt vmcnt(11)
	v_mul_f32_e32 v104, v140, v96
	v_mul_f32_e32 v105, v141, v96
	v_mul_f32_e32 v106, v142, v96
	v_mul_f32_e32 v107, v143, v96
	v_mul_f32_e32 v104, v12, v104
	v_mul_f32_e32 v105, v10, v105
	v_mul_f32_e32 v106, v13, v106
	v_mul_f32_e32 v107, v11, v107
	v_add_f32_e32 v108, 1.0, v188
	v_add_f32_e32 v109, 1.0, v189
	v_add_f32_e32 v110, 1.0, v190
	v_add_f32_e32 v111, 1.0, v191
	v_fma_f32 v104, v108, v104, v230
	v_fma_f32 v105, v109, v105, v231
	v_fma_f32 v106, v110, v106, v232
	v_fma_f32 v107, v111, v107, v233
	v_cvt_pk_bf16_f32 v114, v104, v105
	v_cvt_pk_bf16_f32 v115, v106, v107
	global_store_dwordx2 v[86:87], v[114:115], off offset:1536
	s_waitcnt vmcnt(10)
	v_mul_f32_e32 v104, v144, v96
	v_mul_f32_e32 v105, v145, v96
	v_mul_f32_e32 v106, v146, v96
	v_mul_f32_e32 v107, v147, v96
	v_mul_f32_e32 v104, v16, v104
	v_mul_f32_e32 v105, v14, v105
	v_mul_f32_e32 v106, v17, v106
	v_mul_f32_e32 v107, v15, v107
	v_add_f32_e32 v108, 1.0, v200
	v_add_f32_e32 v109, 1.0, v201
	v_add_f32_e32 v110, 1.0, v202
	v_add_f32_e32 v111, 1.0, v203
	v_fma_f32 v104, v108, v104, v234
	v_fma_f32 v105, v109, v105, v235
	v_fma_f32 v106, v110, v106, v236
	v_fma_f32 v107, v111, v107, v237
	v_cvt_pk_bf16_f32 v112, v104, v105
	v_cvt_pk_bf16_f32 v113, v106, v107
	global_store_dwordx2 v[86:87], v[112:113], off offset:2048
	s_waitcnt vmcnt(9)
	v_mul_f32_e32 v104, v148, v96
	v_mul_f32_e32 v105, v149, v96
	v_mul_f32_e32 v106, v150, v96
	v_mul_f32_e32 v107, v151, v96
	v_mul_f32_e32 v104, v20, v104
	v_mul_f32_e32 v105, v18, v105
	v_mul_f32_e32 v106, v21, v106
	v_mul_f32_e32 v107, v19, v107
	v_add_f32_e32 v108, 1.0, v204
	v_add_f32_e32 v109, 1.0, v205
	v_add_f32_e32 v110, 1.0, v206
	v_add_f32_e32 v111, 1.0, v207
	v_fma_f32 v104, v108, v104, v238
	v_fma_f32 v105, v109, v105, v239
	v_fma_f32 v106, v110, v106, v240
	v_fma_f32 v107, v111, v107, v241
	v_cvt_pk_bf16_f32 v114, v104, v105
	v_cvt_pk_bf16_f32 v115, v106, v107
	global_store_dwordx2 v[86:87], v[114:115], off offset:2560
	s_waitcnt vmcnt(8)
	v_mul_f32_e32 v104, v152, v96
	v_mul_f32_e32 v105, v153, v96
	v_mul_f32_e32 v106, v154, v96
	v_mul_f32_e32 v107, v155, v96
	v_mul_f32_e32 v104, v24, v104
	v_mul_f32_e32 v105, v22, v105
	v_mul_f32_e32 v106, v25, v106
	v_mul_f32_e32 v107, v23, v107
	v_add_f32_e32 v108, 1.0, v208
	v_add_f32_e32 v109, 1.0, v209
	v_add_f32_e32 v110, 1.0, v210
	v_add_f32_e32 v111, 1.0, v211
	v_fma_f32 v104, v108, v104, v242
	v_fma_f32 v105, v109, v105, v243
	v_fma_f32 v106, v110, v106, v244
	v_fma_f32 v107, v111, v107, v245
	v_cvt_pk_bf16_f32 v112, v104, v105
	v_cvt_pk_bf16_f32 v113, v106, v107
	global_store_dwordx2 v[86:87], v[112:113], off offset:3072
	s_waitcnt vmcnt(7)
	v_mul_f32_e32 v104, v156, v96
	v_mul_f32_e32 v105, v157, v96
	v_mul_f32_e32 v106, v158, v96
	v_mul_f32_e32 v107, v159, v96
	v_mul_f32_e32 v104, v28, v104
	v_mul_f32_e32 v105, v26, v105
	v_mul_f32_e32 v106, v29, v106
	v_mul_f32_e32 v107, v27, v107
	v_add_f32_e32 v108, 1.0, v212
	v_add_f32_e32 v109, 1.0, v213
	v_add_f32_e32 v110, 1.0, v214
	v_add_f32_e32 v111, 1.0, v215
	v_fma_f32 v104, v108, v104, v246
	v_fma_f32 v105, v109, v105, v247
	v_fma_f32 v106, v110, v106, v248
	v_fma_f32 v107, v111, v107, v249
	v_cvt_pk_bf16_f32 v114, v104, v105
	v_cvt_pk_bf16_f32 v115, v106, v107
	global_store_dwordx2 v[86:87], v[114:115], off offset:3584
	v_mov_b32_e32 v30, 0x26400
	ds_read_b32 v30, v30 offset:192
	s_waitcnt lgkmcnt(0)
	s_nop 0
	v_readfirstlane_b32 s12, v30
	s_nop 1
	v_lshl_add_u32 v64, s12, 3, v64
	s_movk_i32 s12, 0x40ff
	v_cmp_lt_i32_e32 vcc, s12, v64
	s_or_b64 s[10:11], vcc, s[10:11]
	s_andn2_b64 exec, exec, s[10:11]
	s_cbranch_execnz .LBB0_1679
